# P1 norm row loop: the 21 loads of the 7-step load-wait-store ladder requested with the row's first eleven loads (memory-level parallelism), waits re-derived
# baseline (speedup 1.0000x reference)
.LBB0_231:
	v_lshl_add_u64 v[2:3], s[18:19], 0, v[34:35]
	global_load_dwordx4 v[38:41], v[2:3], off
	global_load_dwordx4 v[42:45], v[2:3], off offset:1024
	global_load_dwordx4 v[46:49], v[2:3], off offset:2048
	global_load_dwordx4 v[18:21], v[2:3], off offset:3072
	v_add_co_u32_e32 v50, vcc, s20, v2
	s_min_i32 s12, s2, 0x8000
	s_nop 0
	v_addc_co_u32_e32 v51, vcc, 0, v3, vcc
	global_load_dwordx4 v[10:13], v[50:51], off
	global_load_dwordx4 v[14:17], v[50:51], off offset:1024
	global_load_dwordx4 v[2:5], v[50:51], off offset:3072
	global_load_dwordx4 v[6:9], v[50:51], off offset:2048
	s_ashr_i32 s12, s12, 13
	s_mul_i32 s18, s12, 0x3000
	s_ashr_i32 s19, s18, 31
	s_lshl_b64 s[18:19], s[18:19], 2
	s_add_u32 s18, s24, s18
	s_addc_u32 s19, s25, s19
	v_lshl_add_u64 v[62:63], s[18:19], 0, v[34:35]
	v_add_co_u32_e32 v64, vcc, s22, v62
	global_load_dwordx4 v[54:57], v[22:23], off
	s_nop 0
	v_addc_co_u32_e32 v65, vcc, 0, v63, vcc
	global_load_dwordx4 v[50:53], v[64:65], off offset:-4096
	global_load_dwordx4 v[58:61], v[62:63], off
	v_lshl_add_u64 v[184:185], v[62:63], 0, s[14:15]
	v_add_co_u32_e32 v186, vcc, s20, v62
	s_nop 1
	v_addc_co_u32_e32 v187, vcc, 0, v63, vcc
	global_load_dwordx4 v[100:103], v[22:23], off offset:1024
	global_load_dwordx4 v[104:107], v[184:185], off offset:1024
	global_load_dwordx4 v[108:111], v[62:63], off offset:1024
	global_load_dwordx4 v[112:115], v[22:23], off offset:2048
	global_load_dwordx4 v[116:119], v[184:185], off offset:2048
	global_load_dwordx4 v[120:123], v[62:63], off offset:2048
	global_load_dwordx4 v[124:127], v[22:23], off offset:3072
	global_load_dwordx4 v[128:131], v[184:185], off offset:3072
	global_load_dwordx4 v[132:135], v[62:63], off offset:3072
	global_load_dwordx4 v[136:139], v[26:27], off
	global_load_dwordx4 v[140:143], v[64:65], off
	global_load_dwordx4 v[144:147], v[186:187], off
	global_load_dwordx4 v[148:151], v[28:29], off
	global_load_dwordx4 v[152:155], v[64:65], off offset:1024
	global_load_dwordx4 v[156:159], v[186:187], off offset:1024
	global_load_dwordx4 v[160:163], v[30:31], off
	global_load_dwordx4 v[164:167], v[64:65], off offset:2048
	global_load_dwordx4 v[168:171], v[186:187], off offset:2048
	global_load_dwordx4 v[172:175], v[32:33], off
	global_load_dwordx4 v[176:179], v[64:65], off offset:3072
	global_load_dwordx4 v[180:183], v[186:187], off offset:3072
	v_mov_b32_e32 v87, 0
	v_mov_b32_e32 v37, 0
	s_lshl_b64 s[16:17], s[16:17], 12
	s_add_u32 s2, s2, s6
	s_addc_u32 s3, s3, s7
	s_add_u32 s8, s8, s10
	s_addc_u32 s9, s9, s11
	s_cmp_lt_i32 s2, 0x8400
	s_waitcnt vmcnt(31)
	v_mov_b32_e32 v68, v39
	s_waitcnt vmcnt(30)
	v_mov_b32_e32 v69, v43
	v_mov_b32_e32 v72, v41
	v_mov_b32_e32 v73, v45
	v_mov_b32_e32 v66, v38
	v_mov_b32_e32 v67, v42
	v_mov_b32_e32 v70, v40
	v_mov_b32_e32 v71, v44
	s_waitcnt vmcnt(29)
	v_pk_mul_f32 v[74:75], v[48:49], v[48:49]
	v_pk_mul_f32 v[76:77], v[46:47], v[46:47]
	v_pk_mul_f32 v[68:69], v[68:69], v[68:69]
	v_pk_mul_f32 v[72:73], v[72:73], v[72:73]
	v_pk_mov_b32 v[82:83], v[76:77], v[74:75] op_sel:[1,0]
	v_mov_b32_e32 v77, v75
	v_pk_fma_f32 v[66:67], v[66:67], v[66:67], v[68:69]
	v_pk_fma_f32 v[68:69], v[70:71], v[70:71], v[72:73]
	s_waitcnt vmcnt(28)
	v_mul_f32_e32 v78, v19, v19
	v_mul_f32_e32 v80, v21, v21
	v_pk_add_f32 v[70:71], v[82:83], v[76:77]
	v_pk_add_f32 v[66:67], v[66:67], v[68:69]
	s_waitcnt vmcnt(27)
	v_mul_f32_e32 v89, v10, v10
	v_mul_f32_e32 v90, v11, v11
	v_mul_f32_e32 v91, v12, v12
	v_mul_f32_e32 v92, v13, v13
	v_pk_fma_f32 v[74:75], v[18:19], v[18:19], v[78:79] op_sel_hi:[1,1,0]
	v_pk_fma_f32 v[78:79], v[20:21], v[20:21], v[80:81] op_sel_hi:[1,1,0]
	v_pk_add_f32 v[68:69], v[70:71], v[70:71] op_sel:[0,1] op_sel_hi:[1,0]
	v_pk_add_f32 v[66:67], v[66:67], v[66:67] op_sel:[0,1] op_sel_hi:[1,0]
	s_waitcnt vmcnt(26)
	v_pk_mul_f32 v[80:81], v[16:17], v[16:17]
	v_pk_mul_f32 v[84:85], v[14:15], v[14:15]
	v_mov_b32_e32 v75, v91
	v_mov_b32_e32 v79, v92
	v_mov_b32_e32 v69, v90
	v_mov_b32_e32 v67, v89
	v_pk_mov_b32 v[72:73], v[84:85], v[80:81] op_sel:[1,0]
	v_mov_b32_e32 v85, v81
	v_pk_add_f32 v[70:71], v[74:75], v[78:79]
	v_pk_add_f32 v[66:67], v[66:67], v[68:69]
	s_waitcnt vmcnt(24)
	v_mul_f32_e32 v86, v7, v7
	v_mul_f32_e32 v88, v9, v9
	v_pk_add_f32 v[72:73], v[72:73], v[84:85]
	v_pk_add_f32 v[66:67], v[66:67], v[70:71]
	v_mul_f32_e32 v93, v2, v2
	v_mul_f32_e32 v94, v3, v3
	v_mul_f32_e32 v95, v4, v4
	v_mul_f32_e32 v96, v5, v5
	v_pk_fma_f32 v[76:77], v[6:7], v[6:7], v[86:87] op_sel_hi:[1,1,0]
	v_pk_fma_f32 v[80:81], v[8:9], v[8:9], v[88:89] op_sel_hi:[1,1,0]
	v_pk_add_f32 v[72:73], v[72:73], v[72:73] op_sel:[0,1] op_sel_hi:[1,0]
	v_pk_add_f32 v[66:67], v[66:67], v[66:67] op_sel:[0,1] op_sel_hi:[1,0]
	v_mov_b32_e32 v77, v95
	v_mov_b32_e32 v81, v96
	v_mov_b32_e32 v73, v94
	v_mov_b32_e32 v67, v93
	v_pk_add_f32 v[74:75], v[76:77], v[80:81]
	v_pk_add_f32 v[66:67], v[66:67], v[72:73]
	s_waitcnt vmcnt(22)
	v_pk_add_f32 v[52:53], v[52:53], 1.0 op_sel_hi:[1,0]
	v_pk_add_f32 v[66:67], v[66:67], v[74:75]
	v_pk_add_f32 v[50:51], v[50:51], 1.0 op_sel_hi:[1,0]
	v_add_f32_e32 v66, v66, v67
	s_nop 1
	v_add_f32_dpp v66, v66, v66 row_shr:1 row_mask:0xf bank_mask:0xf bound_ctrl:1
	s_nop 1
	v_add_f32_dpp v66, v66, v66 row_shr:2 row_mask:0xf bank_mask:0xf bound_ctrl:1
	s_nop 1
	v_add_f32_dpp v66, v66, v66 row_shr:4 row_mask:0xf bank_mask:0xf bound_ctrl:1
	s_nop 1
	v_add_f32_dpp v66, v66, v66 row_shr:8 row_mask:0xf bank_mask:0xf bound_ctrl:1
	s_nop 1
	v_mov_b32_dpp v37, v66 row_bcast:15 row_mask:0xa bank_mask:0xf
	v_add_f32_e32 v37, v66, v37
	s_nop 1
	v_mov_b32_dpp v87, v37 row_bcast:31 row_mask:0xc bank_mask:0xf
	v_add_f32_e32 v37, v37, v87
	s_nop 0
	v_readlane_b32 s12, v37, 63
	s_nop 1
	v_fma_f32 v37, s12, v36, v1
	v_mul_f32_e32 v66, 0x4b800000, v37
	v_cmp_gt_f32_e32 vcc, s21, v37
	s_nop 1
	v_cndmask_b32_e32 v37, v37, v66, vcc
	v_rsq_f32_e32 v37, v37
	v_lshl_add_u64 v[66:67], v[24:25], 0, s[16:17]
	v_mul_f32_e32 v68, 0x45800000, v37
	v_cndmask_b32_e32 v68, v37, v68, vcc
	v_pk_mul_f32 v[40:41], v[40:41], v[68:69] op_sel_hi:[1,0]
	v_pk_mul_f32 v[38:39], v[38:39], v[68:69] op_sel_hi:[1,0]
	v_pk_mul_f32 v[40:41], v[56:57], v[40:41]
	v_pk_mul_f32 v[38:39], v[54:55], v[38:39]
	s_waitcnt vmcnt(21)
	v_pk_fma_f32 v[40:41], v[52:53], v[40:41], v[60:61]
	v_pk_fma_f32 v[38:39], v[50:51], v[38:39], v[58:59]
	v_lshl_add_u64 v[58:59], v[62:63], 0, s[14:15]
	v_cvt_pk_bf16_f32 v38, v38, v39
	v_cvt_pk_bf16_f32 v39, v40, v41
	global_store_dwordx2 v[66:67], v[38:39], off
	v_pk_mul_f32 v[44:45], v[44:45], v[68:69] op_sel_hi:[1,0]
	v_pk_mul_f32 v[42:43], v[42:43], v[68:69] op_sel_hi:[1,0]
	v_pk_mul_f32 v[48:49], v[48:49], v[68:69] op_sel_hi:[1,0]
	v_pk_mul_f32 v[46:47], v[46:47], v[68:69] op_sel_hi:[1,0]
	v_pk_mul_f32 v[20:21], v[20:21], v[68:69] op_sel_hi:[1,0]
	v_pk_mul_f32 v[18:19], v[18:19], v[68:69] op_sel_hi:[1,0]
	v_pk_mul_f32 v[12:13], v[12:13], v[68:69] op_sel_hi:[1,0]
	v_pk_mul_f32 v[10:11], v[10:11], v[68:69] op_sel_hi:[1,0]
	v_pk_mul_f32 v[16:17], v[16:17], v[68:69] op_sel_hi:[1,0]
	v_pk_mul_f32 v[14:15], v[14:15], v[68:69] op_sel_hi:[1,0]
	v_pk_mul_f32 v[8:9], v[8:9], v[68:69] op_sel_hi:[1,0]
	v_pk_mul_f32 v[6:7], v[6:7], v[68:69] op_sel_hi:[1,0]
	v_pk_mul_f32 v[4:5], v[4:5], v[68:69] op_sel_hi:[1,0]
	v_pk_mul_f32 v[2:3], v[2:3], v[68:69] op_sel_hi:[1,0]
	s_waitcnt vmcnt(21)
	v_pk_mul_f32 v[38:39], v[100:101], v[42:43]
	v_pk_mul_f32 v[40:41], v[102:103], v[44:45]
	s_waitcnt vmcnt(20)
	v_pk_add_f32 v[42:43], v[106:107], 1.0 op_sel_hi:[1,0]
	v_pk_add_f32 v[44:45], v[104:105], 1.0 op_sel_hi:[1,0]
	s_waitcnt vmcnt(19)
	v_pk_fma_f32 v[40:41], v[42:43], v[40:41], v[110:111]
	v_pk_fma_f32 v[38:39], v[44:45], v[38:39], v[108:109]
	s_nop 0
	v_cvt_pk_bf16_f32 v38, v38, v39
	v_cvt_pk_bf16_f32 v39, v40, v41
	global_store_dwordx2 v[66:67], v[38:39], off offset:512
	s_waitcnt vmcnt(19)
	v_pk_mul_f32 v[38:39], v[112:113], v[46:47]
	v_pk_mul_f32 v[40:41], v[114:115], v[48:49]
	s_waitcnt vmcnt(18)
	v_pk_add_f32 v[44:45], v[118:119], 1.0 op_sel_hi:[1,0]
	v_pk_add_f32 v[42:43], v[116:117], 1.0 op_sel_hi:[1,0]
	s_waitcnt vmcnt(17)
	v_pk_fma_f32 v[40:41], v[40:41], v[44:45], v[122:123]
	v_pk_fma_f32 v[38:39], v[38:39], v[42:43], v[120:121]
	s_nop 0
	v_cvt_pk_bf16_f32 v38, v38, v39
	v_cvt_pk_bf16_f32 v39, v40, v41
	global_store_dwordx2 v[66:67], v[38:39], off offset:1024
	s_waitcnt vmcnt(17)
	v_pk_mul_f32 v[18:19], v[18:19], v[124:125]
	v_pk_mul_f32 v[20:21], v[20:21], v[126:127]
	s_waitcnt vmcnt(16)
	v_pk_add_f32 v[38:39], v[130:131], 1.0 op_sel_hi:[1,0]
	v_pk_add_f32 v[40:41], v[128:129], 1.0 op_sel_hi:[1,0]
	s_waitcnt vmcnt(15)
	v_pk_fma_f32 v[20:21], v[20:21], v[38:39], v[134:135]
	v_pk_fma_f32 v[18:19], v[18:19], v[40:41], v[132:133]
	v_add_co_u32_e32 v46, vcc, s20, v62
	v_cvt_pk_bf16_f32 v18, v18, v19
	v_cvt_pk_bf16_f32 v19, v20, v21
	global_store_dwordx2 v[66:67], v[18:19], off offset:1536
	v_addc_co_u32_e32 v47, vcc, 0, v63, vcc
	s_waitcnt vmcnt(15)
	v_pk_mul_f32 v[10:11], v[10:11], v[136:137]
	v_pk_mul_f32 v[12:13], v[12:13], v[138:139]
	s_waitcnt vmcnt(14)
	v_pk_add_f32 v[18:19], v[142:143], 1.0 op_sel_hi:[1,0]
	v_pk_add_f32 v[20:21], v[140:141], 1.0 op_sel_hi:[1,0]
	s_waitcnt vmcnt(13)
	v_pk_fma_f32 v[12:13], v[12:13], v[18:19], v[146:147]
	v_pk_fma_f32 v[10:11], v[10:11], v[20:21], v[144:145]
	s_nop 0
	v_cvt_pk_bf16_f32 v10, v10, v11
	v_cvt_pk_bf16_f32 v11, v12, v13
	global_store_dwordx2 v[66:67], v[10:11], off offset:2048
	s_waitcnt vmcnt(13)
	v_pk_mul_f32 v[10:11], v[14:15], v[148:149]
	v_pk_mul_f32 v[12:13], v[16:17], v[150:151]
	s_waitcnt vmcnt(12)
	v_pk_add_f32 v[14:15], v[154:155], 1.0 op_sel_hi:[1,0]
	v_pk_add_f32 v[16:17], v[152:153], 1.0 op_sel_hi:[1,0]
	s_waitcnt vmcnt(11)
	v_pk_fma_f32 v[12:13], v[12:13], v[14:15], v[158:159]
	v_pk_fma_f32 v[10:11], v[10:11], v[16:17], v[156:157]
	s_nop 0
	v_cvt_pk_bf16_f32 v10, v10, v11
	v_cvt_pk_bf16_f32 v11, v12, v13
	global_store_dwordx2 v[66:67], v[10:11], off offset:2560
	s_waitcnt vmcnt(11)
	v_pk_mul_f32 v[6:7], v[6:7], v[160:161]
	v_pk_mul_f32 v[8:9], v[8:9], v[162:163]
	s_waitcnt vmcnt(10)
	v_pk_add_f32 v[10:11], v[166:167], 1.0 op_sel_hi:[1,0]
	v_pk_add_f32 v[12:13], v[164:165], 1.0 op_sel_hi:[1,0]
	s_waitcnt vmcnt(9)
	v_pk_fma_f32 v[8:9], v[8:9], v[10:11], v[170:171]
	v_pk_fma_f32 v[6:7], v[6:7], v[12:13], v[168:169]
	s_nop 0
	v_cvt_pk_bf16_f32 v6, v6, v7
	v_cvt_pk_bf16_f32 v7, v8, v9
	global_store_dwordx2 v[66:67], v[6:7], off offset:3072
	s_waitcnt vmcnt(9)
	v_pk_mul_f32 v[2:3], v[2:3], v[172:173]
	v_pk_mul_f32 v[4:5], v[4:5], v[174:175]
	s_waitcnt vmcnt(8)
	v_pk_add_f32 v[6:7], v[178:179], 1.0 op_sel_hi:[1,0]
	v_pk_add_f32 v[8:9], v[176:177], 1.0 op_sel_hi:[1,0]
	s_waitcnt vmcnt(7)
	v_pk_fma_f32 v[4:5], v[4:5], v[6:7], v[182:183]
	v_pk_fma_f32 v[2:3], v[2:3], v[8:9], v[180:181]
	s_nop 0
	v_cvt_pk_bf16_f32 v2, v2, v3
	v_cvt_pk_bf16_f32 v3, v4, v5
	global_store_dwordx2 v[66:67], v[2:3], off offset:3584
	s_cbranch_scc0 .LBB0_234
